# ping-pong with 4 phases per interval: PV(b) merged with next QK(a) so every step pairs 40 MFMAs with a softmax phase
# speedup vs baseline: 1.0250x; 1.0077x over previous
.Lno_bload:
	v_add_u32_e32 v248, s14, v151
	v_add_u32_e32 v249, s14, v152
	ds_read_b64_tr_b16 v[224:225], v248
	ds_read_b64_tr_b16 v[226:227], v249 offset:768
	ds_read_b64_tr_b16 v[228:229], v248 offset:128
	ds_read_b64_tr_b16 v[230:231], v249 offset:896
	ds_read_b64_tr_b16 v[232:233], v248 offset:6144
	ds_read_b64_tr_b16 v[234:235], v249 offset:6912
	ds_read_b64_tr_b16 v[236:237], v248 offset:6272
	ds_read_b64_tr_b16 v[238:239], v249 offset:7040
	ds_read_b64_tr_b16 v[240:241], v248 offset:12288
	ds_read_b64_tr_b16 v[242:243], v249 offset:13056
	ds_read_b64_tr_b16 v[244:245], v248 offset:12416
	ds_read_b64_tr_b16 v[246:247], v249 offset:13184
	ds_read_b64_tr_b16 v[252:253], v248 offset:18432
	ds_read_b64_tr_b16 v[254:255], v249 offset:19200
	ds_read_b64_tr_b16 v[204:205], v248 offset:18560
	ds_read_b64_tr_b16 v[206:207], v249 offset:19328
	v_exp_f32_e32 v80, v80
	v_exp_f32_e32 v81, v81
	v_exp_f32_e32 v82, v82
	v_exp_f32_e32 v83, v83
	v_add_f32_e32 v146, 0, v80
	v_exp_f32_e32 v84, v84
	v_add_f32_e32 v146, v81, v146
	v_exp_f32_e32 v85, v85
	v_add_f32_e32 v146, v82, v146
	v_exp_f32_e32 v86, v86
	v_add_f32_e32 v146, v83, v146
	v_exp_f32_e32 v87, v87
	v_add_f32_e32 v146, v84, v146
	v_exp_f32_e32 v88, v88
	v_add_f32_e32 v146, v85, v146
	v_exp_f32_e32 v89, v89
	v_add_f32_e32 v146, v86, v146
	v_exp_f32_e32 v90, v90
	v_add_f32_e32 v146, v87, v146
	v_exp_f32_e32 v91, v91
	v_add_f32_e32 v146, v88, v146
	v_exp_f32_e32 v92, v92
	v_add_f32_e32 v146, v89, v146
	v_exp_f32_e32 v93, v93
	v_add_f32_e32 v146, v90, v146
	v_exp_f32_e32 v94, v94
	v_add_f32_e32 v146, v91, v146
	v_exp_f32_e32 v95, v95
	v_add_f32_e32 v146, v92, v146
	v_exp_f32_e32 v64, v64
	v_add_f32_e32 v146, v93, v146
	v_exp_f32_e32 v65, v65
	v_add_f32_e32 v146, v94, v146
	v_exp_f32_e32 v66, v66
	v_add_f32_e32 v146, v95, v146
	v_exp_f32_e32 v67, v67
	v_add_f32_e32 v146, v64, v146
	v_exp_f32_e32 v68, v68
	v_add_f32_e32 v146, v65, v146
	v_exp_f32_e32 v69, v69
	v_add_f32_e32 v146, v66, v146
	v_exp_f32_e32 v70, v70
	v_add_f32_e32 v146, v67, v146
	v_exp_f32_e32 v71, v71
	v_add_f32_e32 v146, v68, v146
	v_exp_f32_e32 v161, v72
	v_add_f32_e32 v146, v69, v146
	v_add_f32_e32 v146, v70, v146
	v_add_f32_e32 v146, v71, v146
	v_add_f32_e32 v72, v161, v146
	v_exp_f32_e32 v146, v73
	v_exp_f32_e32 v162, v74
	v_exp_f32_e32 v163, v75
	v_exp_f32_e32 v164, v76
	v_add_f32_e32 v72, v146, v72
	v_exp_f32_e32 v165, v77
	v_add_f32_e32 v72, v162, v72
	v_exp_f32_e32 v166, v78
	v_add_f32_e32 v72, v163, v72
	v_exp_f32_e32 v167, v79
	v_add_f32_e32 v72, v164, v72
	v_add_f32_e32 v72, v165, v72
	v_add_f32_e32 v72, v166, v72
	v_cvt_pk_bf16_f32 v76, v80, v81
	v_cvt_pk_bf16_f32 v77, v84, v85
	v_cvt_pk_bf16_f32 v78, v82, v83
	v_cvt_pk_bf16_f32 v79, v86, v87
	v_cvt_pk_bf16_f32 v64, v64, v65
	v_cvt_pk_bf16_f32 v65, v68, v69
	v_cvt_pk_bf16_f32 v68, v161, v146
	v_add_f32_e32 v159, v167, v72
	v_cvt_pk_bf16_f32 v72, v88, v89
	v_cvt_pk_bf16_f32 v73, v92, v93
	v_cvt_pk_bf16_f32 v74, v90, v91
	v_cvt_pk_bf16_f32 v75, v94, v95
	v_cvt_pk_bf16_f32 v66, v66, v67
	v_cvt_pk_bf16_f32 v67, v70, v71
	v_cvt_pk_bf16_f32 v71, v166, v167
	v_cvt_pk_bf16_f32 v69, v164, v165
	v_cvt_pk_bf16_f32 v70, v162, v163
	v_add_u32_e32 v166, s14, v153
	v_add_u32_e32 v167, s14, v154
	s_barrier
	s_add_i32 s14, s10, -2
	s_and_b32 s14, s14, 3
	s_mulk_i32 s14, 0x6000
	v_add_u32_e32 v146, s14, v147
	v_add_u32_e32 v161, s14, v148
	v_add_u32_e32 v144, s14, v149
	v_add_u32_e32 v168, s14, v150
	s_waitcnt lgkmcnt(14)
	v_mfma_f32_32x32x16_bf16 v[48:63], v[224:227], v[76:79], v[48:63]
	ds_read_b64_tr_b16 v[224:225], v166
	ds_read_b64_tr_b16 v[226:227], v167 offset:768
	s_waitcnt lgkmcnt(14)
	v_mfma_f32_32x32x16_bf16 v[0:15], v[228:231], v[76:79], v[0:15]
	ds_read_b64_tr_b16 v[228:229], v166 offset:128
	ds_read_b64_tr_b16 v[230:231], v167 offset:896
	s_waitcnt lgkmcnt(14)
	v_mfma_f32_32x32x16_bf16 v[48:63], v[232:235], v[72:75], v[48:63]
	ds_read_b64_tr_b16 v[232:233], v166 offset:6144
	ds_read_b64_tr_b16 v[234:235], v167 offset:6912
	s_waitcnt lgkmcnt(14)
	v_mfma_f32_32x32x16_bf16 v[0:15], v[236:239], v[72:75], v[0:15]
	ds_read_b64_tr_b16 v[236:237], v166 offset:6272
	ds_read_b64_tr_b16 v[238:239], v167 offset:7040
	s_waitcnt lgkmcnt(14)
	v_mfma_f32_32x32x16_bf16 v[48:63], v[240:243], v[64:67], v[48:63]
	ds_read_b64_tr_b16 v[240:241], v166 offset:12288
	ds_read_b64_tr_b16 v[242:243], v167 offset:13056
	s_waitcnt lgkmcnt(14)
	v_mfma_f32_32x32x16_bf16 v[0:15], v[244:247], v[64:67], v[0:15]
	ds_read_b64_tr_b16 v[244:245], v166 offset:12416
	ds_read_b64_tr_b16 v[246:247], v167 offset:13184
	s_waitcnt lgkmcnt(14)
	v_mfma_f32_32x32x16_bf16 v[48:63], v[252:255], v[68:71], v[48:63]
	ds_read_b64_tr_b16 v[252:253], v166 offset:18432
	ds_read_b64_tr_b16 v[254:255], v167 offset:19200
	s_waitcnt lgkmcnt(14)
	v_mfma_f32_32x32x16_bf16 v[0:15], v[204:207], v[68:71], v[0:15]
	ds_read_b64_tr_b16 v[204:205], v166 offset:18560
	ds_read_b64_tr_b16 v[206:207], v167 offset:19328
	s_waitcnt lgkmcnt(14)
	v_mfma_f32_32x32x16_bf16 v[32:47], v[224:227], v[76:79], v[32:47]
	ds_read_b128 v[224:227], v146
	s_waitcnt lgkmcnt(13)
	v_mfma_f32_32x32x16_bf16 v[16:31], v[228:231], v[76:79], v[16:31]
	ds_read_b128 v[228:231], v146 offset:12288
	s_waitcnt lgkmcnt(12)
	v_mfma_f32_32x32x16_bf16 v[32:47], v[232:235], v[72:75], v[32:47]
	ds_read_b128 v[232:235], v161
	s_waitcnt lgkmcnt(11)
	v_mfma_f32_32x32x16_bf16 v[16:31], v[236:239], v[72:75], v[16:31]
	ds_read_b128 v[236:239], v161 offset:12288
	s_waitcnt lgkmcnt(10)
	v_mfma_f32_32x32x16_bf16 v[32:47], v[240:243], v[64:67], v[32:47]
	ds_read_b128 v[240:243], v144
	s_waitcnt lgkmcnt(9)
	v_mfma_f32_32x32x16_bf16 v[16:31], v[244:247], v[64:67], v[16:31]
	ds_read_b128 v[244:247], v144 offset:12288
	s_waitcnt lgkmcnt(8)
	v_mfma_f32_32x32x16_bf16 v[32:47], v[252:255], v[68:71], v[32:47]
	ds_read_b128 v[252:255], v168
	s_waitcnt lgkmcnt(7)
	v_mfma_f32_32x32x16_bf16 v[16:31], v[204:207], v[68:71], v[16:31]
	ds_read_b128 v[204:207], v168 offset:12288
	s_waitcnt lgkmcnt(7)
	v_mfma_f32_32x32x16_bf16 v[80:95], v[224:227], v[112:115], 0
	ds_read_b128 v[224:227], v146 offset:128
	s_waitcnt lgkmcnt(7)
	v_mfma_f32_32x32x16_bf16 v[64:79], v[228:231], v[112:115], 0
	ds_read_b128 v[228:231], v146 offset:12416
	s_waitcnt lgkmcnt(7)
	v_mfma_f32_32x32x16_bf16 v[80:95], v[232:235], v[116:119], v[80:95]
	ds_read_b128 v[232:235], v161 offset:128
	s_waitcnt lgkmcnt(7)
	v_mfma_f32_32x32x16_bf16 v[64:79], v[236:239], v[116:119], v[64:79]
	ds_read_b128 v[236:239], v161 offset:12416
	s_waitcnt lgkmcnt(7)
	v_mfma_f32_32x32x16_bf16 v[80:95], v[240:243], v[120:123], v[80:95]
	ds_read_b128 v[240:243], v144 offset:128
	s_waitcnt lgkmcnt(7)
	v_mfma_f32_32x32x16_bf16 v[64:79], v[244:247], v[120:123], v[64:79]
	ds_read_b128 v[244:247], v144 offset:12416
	s_waitcnt lgkmcnt(7)
	v_mfma_f32_32x32x16_bf16 v[80:95], v[252:255], v[124:127], v[80:95]
	ds_read_b128 v[252:255], v168 offset:128
	s_waitcnt lgkmcnt(7)
	v_mfma_f32_32x32x16_bf16 v[64:79], v[204:207], v[124:127], v[64:79]
	ds_read_b128 v[204:207], v168 offset:12416
	s_waitcnt lgkmcnt(7)
	v_mfma_f32_32x32x16_bf16 v[80:95], v[224:227], v[96:99], v[80:95]
	ds_read_b128 v[224:227], v146 offset:256
	s_waitcnt lgkmcnt(7)
	v_mfma_f32_32x32x16_bf16 v[64:79], v[228:231], v[96:99], v[64:79]
	ds_read_b128 v[228:231], v146 offset:12544
	s_waitcnt lgkmcnt(7)
	v_mfma_f32_32x32x16_bf16 v[80:95], v[232:235], v[100:103], v[80:95]
	ds_read_b128 v[232:235], v161 offset:256
	s_waitcnt lgkmcnt(7)
	v_mfma_f32_32x32x16_bf16 v[64:79], v[236:239], v[100:103], v[64:79]
	ds_read_b128 v[236:239], v161 offset:12544
	s_waitcnt lgkmcnt(7)
	v_mfma_f32_32x32x16_bf16 v[80:95], v[240:243], v[104:107], v[80:95]
	ds_read_b128 v[240:243], v144 offset:256
	s_waitcnt lgkmcnt(7)
	v_mfma_f32_32x32x16_bf16 v[64:79], v[244:247], v[104:107], v[64:79]
	ds_read_b128 v[244:247], v144 offset:12544
	s_waitcnt lgkmcnt(7)
	v_mfma_f32_32x32x16_bf16 v[80:95], v[252:255], v[108:111], v[80:95]
	ds_read_b128 v[252:255], v168 offset:256
	s_waitcnt lgkmcnt(7)
	v_mfma_f32_32x32x16_bf16 v[64:79], v[204:207], v[108:111], v[64:79]
	ds_read_b128 v[204:207], v168 offset:12544
	s_waitcnt lgkmcnt(7)
	v_mfma_f32_32x32x16_bf16 v[80:95], v[224:227], v[128:131], v[80:95]
	s_waitcnt lgkmcnt(6)
	v_mfma_f32_32x32x16_bf16 v[64:79], v[228:231], v[128:131], v[64:79]
	s_waitcnt lgkmcnt(5)
	v_mfma_f32_32x32x16_bf16 v[80:95], v[232:235], v[132:135], v[80:95]
	s_waitcnt lgkmcnt(4)
	v_mfma_f32_32x32x16_bf16 v[64:79], v[236:239], v[132:135], v[64:79]
	s_waitcnt lgkmcnt(3)
	v_mfma_f32_32x32x16_bf16 v[80:95], v[240:243], v[136:139], v[80:95]
	s_waitcnt lgkmcnt(2)
	v_mfma_f32_32x32x16_bf16 v[64:79], v[244:247], v[136:139], v[64:79]
	s_waitcnt lgkmcnt(1)
	v_mfma_f32_32x32x16_bf16 v[80:95], v[252:255], v[140:143], v[80:95]
	s_waitcnt lgkmcnt(0)
	v_mfma_f32_32x32x16_bf16 v[64:79], v[204:207], v[140:143], v[64:79]
	s_waitcnt vmcnt(0)
	s_barrier
	s_cmp_le_u32 s7, s44
	s_cbranch_scc1 .Lf_b
	v_add_u32_e32 v146, 59, v156
	v_cmp_le_i32_e64 s[16:17], 0, v146
	v_cmp_le_i32_e64 s[18:19], 32, v146
	v_cmp_le_i32_e64 vcc, 1, v146
	s_nop 4
	v_cndmask_b32_e64 v80, v199, v80, s[16:17]
	v_cmp_le_i32_e64 s[16:17], 33, v146
	v_cndmask_b32_e64 v64, v199, v64, s[18:19]
	v_cmp_le_i32_e64 s[18:19], 2, v146
	v_cndmask_b32_e64 v81, v199, v81, vcc
	v_cmp_le_i32_e64 vcc, 34, v146
	v_cndmask_b32_e64 v65, v199, v65, s[16:17]
	v_cmp_le_i32_e64 s[16:17], 3, v146
	v_cndmask_b32_e64 v82, v199, v82, s[18:19]
	v_cmp_le_i32_e64 s[18:19], 35, v146
	v_cndmask_b32_e64 v66, v199, v66, vcc
	v_cmp_le_i32_e64 vcc, 8, v146
	v_cndmask_b32_e64 v83, v199, v83, s[16:17]
	v_cmp_le_i32_e64 s[16:17], 40, v146
	v_cndmask_b32_e64 v67, v199, v67, s[18:19]
	v_cmp_le_i32_e64 s[18:19], 9, v146
	v_cndmask_b32_e64 v84, v199, v84, vcc
	v_cmp_le_i32_e64 vcc, 41, v146
	v_cndmask_b32_e64 v68, v199, v68, s[16:17]
	v_cmp_le_i32_e64 s[16:17], 10, v146
	v_cndmask_b32_e64 v85, v199, v85, s[18:19]
	v_cmp_le_i32_e64 s[18:19], 42, v146
	v_cndmask_b32_e64 v69, v199, v69, vcc
	v_cmp_le_i32_e64 vcc, 11, v146
	v_cndmask_b32_e64 v86, v199, v86, s[16:17]
	v_cmp_le_i32_e64 s[16:17], 43, v146
	v_cndmask_b32_e64 v70, v199, v70, s[18:19]
	v_cmp_le_i32_e64 s[18:19], 16, v146
	v_cndmask_b32_e64 v87, v199, v87, vcc
	v_cmp_le_i32_e64 vcc, 48, v146
	v_cndmask_b32_e64 v71, v199, v71, s[16:17]
	v_cmp_le_i32_e64 s[16:17], 17, v146
	v_cndmask_b32_e64 v88, v199, v88, s[18:19]
	v_cmp_le_i32_e64 s[18:19], 49, v146
	v_cndmask_b32_e64 v72, v199, v72, vcc
	v_cmp_le_i32_e64 vcc, 18, v146
	v_cndmask_b32_e64 v89, v199, v89, s[16:17]
	v_cmp_le_i32_e64 s[16:17], 50, v146
	v_cndmask_b32_e64 v73, v199, v73, s[18:19]
	v_cmp_le_i32_e64 s[18:19], 19, v146
	v_cndmask_b32_e64 v90, v199, v90, vcc
	v_cmp_le_i32_e64 vcc, 51, v146
	v_cndmask_b32_e64 v74, v199, v74, s[16:17]
	v_cmp_le_i32_e64 s[16:17], 24, v146
	v_cndmask_b32_e64 v91, v199, v91, s[18:19]
	v_cmp_le_i32_e64 s[18:19], 56, v146
	v_cndmask_b32_e64 v75, v199, v75, vcc
	v_cmp_le_i32_e64 vcc, 25, v146
	v_cndmask_b32_e64 v92, v199, v92, s[16:17]
	v_cmp_le_i32_e64 s[16:17], 57, v146
	v_cndmask_b32_e64 v76, v199, v76, s[18:19]
	v_cmp_le_i32_e64 s[18:19], 26, v146
	v_cndmask_b32_e64 v93, v199, v93, vcc
	v_cmp_le_i32_e64 vcc, 58, v146
	v_cndmask_b32_e64 v77, v199, v77, s[16:17]
	v_cmp_le_i32_e64 s[16:17], 27, v146
	v_cndmask_b32_e64 v94, v199, v94, s[18:19]
	v_cmp_le_i32_e64 s[18:19], 59, v146
	v_cndmask_b32_e64 v78, v199, v78, vcc
	v_cndmask_b32_e64 v95, v199, v95, s[16:17]
	v_cndmask_b32_e64 v79, v199, v79, s[18:19]

.Lno_bload2:
	v_add_u32_e32 v209, s14, v151
	v_add_u32_e32 v210, s14, v152
	v_add_u32_e32 v213, s14, v153
	v_add_u32_e32 v214, s14, v154
	ds_read_b64_tr_b16 v[224:225], v209
	ds_read_b64_tr_b16 v[226:227], v210 offset:768
	ds_read_b64_tr_b16 v[228:229], v209 offset:6144
	ds_read_b64_tr_b16 v[230:231], v210 offset:6912
	ds_read_b64_tr_b16 v[232:233], v209 offset:12288
	ds_read_b64_tr_b16 v[234:235], v210 offset:13056
	ds_read_b64_tr_b16 v[236:237], v209 offset:18432
	ds_read_b64_tr_b16 v[238:239], v210 offset:19200
	ds_read_b64_tr_b16 v[240:241], v213
	ds_read_b64_tr_b16 v[242:243], v214 offset:768
	ds_read_b64_tr_b16 v[244:245], v213 offset:6144
	ds_read_b64_tr_b16 v[246:247], v214 offset:6912
	v_exp_f32_e32 v170, v64
	v_exp_f32_e32 v171, v65
	v_exp_f32_e32 v176, v66
	v_exp_f32_e32 v177, v67
	v_exp_f32_e32 v178, v68
	v_exp_f32_e32 v179, v69
	v_exp_f32_e32 v161, v80
	v_exp_f32_e32 v185, v70
	v_exp_f32_e32 v162, v81
	v_exp_f32_e32 v187, v71
	v_exp_f32_e32 v163, v82
	v_exp_f32_e32 v203, v72
	v_exp_f32_e32 v164, v83
	v_exp_f32_e32 v204, v73
	v_exp_f32_e32 v165, v84
	v_exp_f32_e32 v205, v74
	v_exp_f32_e32 v166, v85
	v_exp_f32_e32 v206, v75
	v_exp_f32_e32 v167, v86
	v_exp_f32_e32 v207, v76
	v_exp_f32_e32 v168, v87
	v_exp_f32_e32 v208, v77
	v_exp_f32_e32 v88, v88
	v_exp_f32_e32 v89, v89
	v_exp_f32_e32 v90, v90
	v_exp_f32_e32 v91, v91
	v_cvt_pk_bf16_f32 v72, v161, v162
	v_cvt_pk_bf16_f32 v73, v165, v166
	v_cvt_pk_bf16_f32 v74, v163, v164
	v_cvt_pk_bf16_f32 v75, v167, v168
	v_exp_f32_e32 v92, v92
	v_exp_f32_e32 v93, v93
	v_exp_f32_e32 v94, v94
	v_exp_f32_e32 v95, v95
	v_exp_f32_e32 v211, v78
	v_mov_b32_e32 v80, v79
	v_cvt_pk_bf16_f32 v76, v88, v89
	v_cvt_pk_bf16_f32 v77, v92, v93
	v_cvt_pk_bf16_f32 v78, v90, v91
	v_cvt_pk_bf16_f32 v79, v94, v95
	v_cvt_pk_bf16_f32 v68, v170, v171
	v_cvt_pk_bf16_f32 v69, v178, v179
	v_cvt_pk_bf16_f32 v70, v176, v177
	v_cvt_pk_bf16_f32 v71, v185, v187
	v_exp_f32_e32 v212, v80
	v_cvt_pk_bf16_f32 v64, v203, v204
	v_cvt_pk_bf16_f32 v65, v207, v208
	v_cvt_pk_bf16_f32 v66, v205, v206
	v_cvt_pk_bf16_f32 v67, v211, v212
	v_add_f32_e32 v158, v158, v159
	s_addk_i32 s12, 0x1000
	s_add_i32 s11, s11, 4
	s_add_i32 s10, s10, 2
	s_addk_i32 s7, 0x80
	v_add_u32_e32 v155, 32, v155
	s_cmp_ge_u32 s13, s9
	v_add_u32_e32 v156, 0xffffff80, v156
	v_add_f32_e32 v84, 0, v161
	v_add_f32_e32 v84, v162, v84
	v_add_f32_e32 v84, v163, v84
	v_add_f32_e32 v84, v164, v84
	v_add_f32_e32 v144, v165, v84
	v_add_f32_e32 v80, v166, v144
	v_add_f32_e32 v80, v167, v80
	v_add_f32_e32 v80, v168, v80
	v_add_f32_e32 v80, v88, v80
	v_add_f32_e32 v88, v89, v80
	v_add_f32_e32 v84, v90, v88
	v_add_f32_e32 v84, v91, v84
	v_add_f32_e32 v84, v92, v84
	v_add_f32_e32 v84, v93, v84
	v_add_f32_e32 v88, v94, v84
	v_add_f32_e32 v80, v95, v88
	v_add_f32_e32 v80, v170, v80
	v_add_f32_e32 v80, v171, v80
	v_add_f32_e32 v80, v176, v80
	v_add_f32_e32 v88, v177, v80
	v_add_f32_e32 v248, v178, v88
	v_add_f32_e32 v249, v179, v248
	v_add_f32_e32 v252, v185, v249
	v_add_f32_e32 v253, v187, v252
	v_add_f32_e32 v84, v203, v253
	v_add_f32_e32 v254, v204, v84
	v_add_f32_e32 v255, v205, v254
	v_add_f32_e32 v248, v206, v255
	v_add_f32_e32 v249, v207, v248
	v_add_f32_e32 v80, v208, v249
	v_add_f32_e32 v252, v211, v80
	v_add_f32_e32 v253, v212, v252
	v_add_f32_e32 v158, v158, v253
	s_barrier
	s_waitcnt lgkmcnt(10)
	v_mfma_f32_32x32x16_bf16 v[48:63], v[224:227], v[72:75], v[48:63]
	ds_read_b64_tr_b16 v[224:225], v213 offset:12288
	ds_read_b64_tr_b16 v[226:227], v214 offset:13056
	s_waitcnt lgkmcnt(10)
	v_mfma_f32_32x32x16_bf16 v[48:63], v[228:231], v[76:79], v[48:63]
	ds_read_b64_tr_b16 v[228:229], v213 offset:18432
	ds_read_b64_tr_b16 v[230:231], v214 offset:19200
	s_waitcnt lgkmcnt(10)
	v_mfma_f32_32x32x16_bf16 v[48:63], v[232:235], v[68:71], v[48:63]
	ds_read_b64_tr_b16 v[232:233], v209 offset:128
	ds_read_b64_tr_b16 v[234:235], v210 offset:896
	s_waitcnt lgkmcnt(10)
	v_mfma_f32_32x32x16_bf16 v[48:63], v[236:239], v[64:67], v[48:63]
	ds_read_b64_tr_b16 v[236:237], v209 offset:6272
	ds_read_b64_tr_b16 v[238:239], v210 offset:7040
	s_waitcnt lgkmcnt(10)
	v_mfma_f32_32x32x16_bf16 v[32:47], v[240:243], v[72:75], v[32:47]
	ds_read_b64_tr_b16 v[240:241], v209 offset:12416
	ds_read_b64_tr_b16 v[242:243], v210 offset:13184
	s_waitcnt lgkmcnt(10)
	v_mfma_f32_32x32x16_bf16 v[32:47], v[244:247], v[76:79], v[32:47]
	ds_read_b64_tr_b16 v[244:245], v209 offset:18560
	ds_read_b64_tr_b16 v[246:247], v210 offset:19328
	s_waitcnt lgkmcnt(10)
	v_mfma_f32_32x32x16_bf16 v[32:47], v[224:227], v[68:71], v[32:47]
	ds_read_b64_tr_b16 v[224:225], v213 offset:128
	ds_read_b64_tr_b16 v[226:227], v214 offset:896
	s_waitcnt lgkmcnt(10)
	v_mfma_f32_32x32x16_bf16 v[32:47], v[228:231], v[64:67], v[32:47]
	ds_read_b64_tr_b16 v[228:229], v213 offset:6272
	ds_read_b64_tr_b16 v[230:231], v214 offset:7040
	s_waitcnt lgkmcnt(10)
	v_mfma_f32_32x32x16_bf16 v[0:15], v[232:235], v[72:75], v[0:15]
	ds_read_b64_tr_b16 v[232:233], v213 offset:12416
	ds_read_b64_tr_b16 v[234:235], v214 offset:13184
	s_waitcnt lgkmcnt(10)
	v_mfma_f32_32x32x16_bf16 v[0:15], v[236:239], v[76:79], v[0:15]
	ds_read_b64_tr_b16 v[236:237], v213 offset:18560
	ds_read_b64_tr_b16 v[238:239], v214 offset:19328
	s_waitcnt lgkmcnt(10)
	v_mfma_f32_32x32x16_bf16 v[0:15], v[240:243], v[68:71], v[0:15]
	s_waitcnt lgkmcnt(8)
	v_mfma_f32_32x32x16_bf16 v[0:15], v[244:247], v[64:67], v[0:15]
	s_waitcnt lgkmcnt(6)
	v_mfma_f32_32x32x16_bf16 v[16:31], v[224:227], v[72:75], v[16:31]
	s_waitcnt lgkmcnt(4)
	v_mfma_f32_32x32x16_bf16 v[16:31], v[228:231], v[76:79], v[16:31]
	s_waitcnt lgkmcnt(2)
	v_mfma_f32_32x32x16_bf16 v[16:31], v[232:235], v[68:71], v[16:31]
	s_waitcnt lgkmcnt(0)
	v_mfma_f32_32x32x16_bf16 v[16:31], v[236:239], v[64:67], v[16:31]
	s_cbranch_scc1 .LBB0_1250
	s_branch .LBB0_1238
